# P9/P12 start stagger in 8 groups ((bid&7) x 1 / x 2 sleep steps) instead of 4 groups
# speedup vs baseline: 1.0010x; 1.0010x over previous
.LBB0_1169:
.LBB0_1170:
	s_cmp_lt_i32 s26, 32
	s_cbranch_scc1 .Lstag9_done
	s_and_b32 s98, s26, 7
	s_mul_i32 s98, s98, 1
	s_cmp_eq_u32 s98, 0
	s_cbranch_scc1 .Lstag9_done

.LBB0_1589:
.LBB0_1590:
	s_cmp_lt_i32 s26, 32
	s_cbranch_scc1 .Lstag12_done
	s_and_b32 s98, s26, 7
	s_mul_i32 s98, s98, 2
	s_cmp_eq_u32 s98, 0
	s_cbranch_scc1 .Lstag12_done
